# baseline (speedup 1.0000x reference)
.LBB1_18:
	s_lshl_b64 s[6:7], s[10:11], 20
	s_add_u32 s3, s12, s6
	s_addc_u32 s5, s13, s7
	s_lshl_b32 s10, s2, 2
	v_lshlrev_b32_e32 v0, 7, v194
	s_add_u32 s10, s3, s10
	v_and_b32_e32 v0, 0xfffffc00, v0
	s_addc_u32 s11, s5, 0
	v_ashrrev_i32_e32 v1, 31, v0
	v_lshl_add_u64 v[2:3], v[0:1], 2, s[10:11]
	v_and_b32_e32 v0, 28, v195
	v_lshlrev_b32_e32 v0, 2, v0
	v_mov_b32_e32 v1, 0
	v_lshl_add_u64 v[96:97], v[2:3], 0, v[0:1]
	s_mov_b64 s[44:45], s[10:11]
	v_lshlrev_b32_e32 v226, 9, v194
	v_and_b32_e32 v227, 7, v194
	s_waitcnt vmcnt(0)
	s_mov_b32 s5, 0x10000
	v_and_b32_e32 v226, 0x7000, v226
	v_lshl_or_b32 v226, v227, 4, v226
	v_and_b32_e32 v0, 12, v195
	v_bitop3_b32 v0, v0, v197, v198 bitop3:0x36
	v_lshlrev_b32_e32 v0, 4, v0
	v_lshl_add_u32 v2, v196, 9, 0
	s_movk_i32 s10, 0x60
	s_waitcnt vmcnt(13)
	v_xad_u32 v83, v0, s10, v2
	s_movk_i32 s10, 0x80
	s_waitcnt vmcnt(12)
	v_xad_u32 v84, v0, s10, v2
	s_movk_i32 s10, 0xa0
	v_xad_u32 v85, v0, s10, v2
	s_movk_i32 s10, 0xc0
	v_xad_u32 v86, v0, s10, v2
	s_movk_i32 s10, 0xe0
	v_xad_u32 v87, v0, s10, v2
	s_lshl_b32 s10, s22, 8
	s_add_i32 s10, s10, 0
	s_lshl_b32 s11, s22, 12
	v_add_u32_e32 v98, s10, v195
	s_lshl_b32 s10, s22, 2
	s_add_i32 s11, s11, 0
	v_add_u32_e32 v80, v2, v0
	v_xad_u32 v81, v0, 32, v2
	v_xad_u32 v82, v0, 64, v2
	s_add_i32 s10, s10, 0
	v_lshl_add_u32 v0, v194, 4, s11
	s_mov_b32 s3, 0
	v_add_u32_e32 v88, 0x20000, v98
	s_add_i32 s10, s10, 0x20800
	v_add_u32_e32 v89, 0x18000, v0
	s_setprio 1
	v_add_u32_e32 v0, 0x8000, v80
	ds_read_b128 v[2:5], v0
	ds_read_b128 v[18:21], v0 offset:256
	ds_read_b128 v[22:25], v0 offset:16384
	s_waitcnt vmcnt(8)
	ds_read_b128 v[34:37], v0 offset:16640
	v_add_u32_e32 v0, 0x8000, v81
	ds_read_b128 v[26:29], v0
	ds_read_b128 v[30:33], v0 offset:256
	ds_read_b128 v[38:41], v0 offset:16384
	ds_read_b128 v[42:45], v0 offset:16640
	global_load_dwordx4 v[52:55], v226, s[44:45] nt
	s_add_u32 s46, s44, 0x8000
	s_addc_u32 s47, s45, 0
	global_load_dwordx4 v[60:63], v226, s[46:47] nt
	s_add_u32 s46, s44, 0x10000
	s_addc_u32 s47, s45, 0
	global_load_dwordx4 v[76:79], v226, s[46:47] nt
	s_add_u32 s46, s44, 0x18000
	s_addc_u32 s47, s45, 0
	global_load_dwordx4 v[64:67], v226, s[46:47] nt
	s_add_u32 s46, s44, 0x40000
	s_addc_u32 s47, s45, 0
	global_load_dwordx4 v[68:71], v226, s[46:47] nt
	s_add_u32 s46, s44, 0x48000
	s_addc_u32 s47, s45, 0
	global_load_dwordx4 v[72:75], v226, s[46:47] nt
	s_add_u32 s46, s44, 0x50000
	s_addc_u32 s47, s45, 0
	global_load_dwordx4 v[56:59], v226, s[46:47] nt
	s_add_u32 s46, s44, 0x58000
	s_addc_u32 s47, s45, 0
	global_load_dwordx4 v[48:51], v226, s[46:47] nt
	s_waitcnt lgkmcnt(4)
	v_add_u32_e32 v0, 0x8000, v82
	v_mfma_f32_32x32x16_bf16 v[2:17], v[2:5], v[128:131], 0
	s_waitcnt lgkmcnt(0)
	v_mfma_f32_32x32x16_bf16 v[2:17], v[18:21], v[160:163], v[2:17]
	ds_read_b128 v[18:21], v0
	ds_read_b128 v[90:93], v0 offset:256
	ds_read_b128 v[100:103], v0 offset:16384
	ds_read_b128 v[104:107], v0 offset:16640
	s_waitcnt lgkmcnt(4)
	v_add_u32_e32 v0, 0x8000, v83
	v_mfma_f32_32x32x16_bf16 v[2:17], v[26:29], v[132:135], v[2:17]
	ds_read_b128 v[26:29], v0
	v_mfma_f32_32x32x16_bf16 v[2:17], v[30:33], v[164:167], v[2:17]
	ds_read_b128 v[30:33], v0 offset:256
	ds_read_b128 v[108:111], v0 offset:16384
	ds_read_b128 v[112:115], v0 offset:16640
	s_waitcnt lgkmcnt(4)
	v_add_u32_e32 v0, 0x8000, v84
	v_mfma_f32_32x32x16_bf16 v[2:17], v[18:21], v[136:139], v[2:17]
	ds_read_b128 v[18:21], v0
	v_mfma_f32_32x32x16_bf16 v[2:17], v[90:93], v[168:171], v[2:17]
	ds_read_b128 v[90:93], v0 offset:256
	ds_read_b128 v[116:119], v0 offset:16384
	ds_read_b128 v[120:123], v0 offset:16640
	s_waitcnt lgkmcnt(4)
	v_add_u32_e32 v0, 0x8000, v85
	v_mfma_f32_32x32x16_bf16 v[2:17], v[26:29], v[140:143], v[2:17]
	ds_read_b128 v[26:29], v0
	v_mfma_f32_32x32x16_bf16 v[2:17], v[30:33], v[172:175], v[2:17]
	ds_read_b128 v[30:33], v0 offset:256
	ds_read_b128 v[124:127], v0 offset:16384
	ds_read_b128 v[194:197], v0 offset:16640
	s_waitcnt lgkmcnt(4)
	v_add_u32_e32 v0, 0x8000, v86
	v_mfma_f32_32x32x16_bf16 v[2:17], v[18:21], v[144:147], v[2:17]
	ds_read_b128 v[18:21], v0
	v_mfma_f32_32x32x16_bf16 v[2:17], v[90:93], v[176:179], v[2:17]
	ds_read_b128 v[90:93], v0 offset:256
	ds_read_b128 v[198:201], v0 offset:16384
	ds_read_b128 v[202:205], v0 offset:16640
	s_waitcnt lgkmcnt(4)
	v_add_u32_e32 v0, 0x8000, v87
	v_mfma_f32_32x32x16_bf16 v[2:17], v[26:29], v[148:151], v[2:17]
	ds_read_b128 v[26:29], v0
	v_mfma_f32_32x32x16_bf16 v[2:17], v[30:33], v[180:183], v[2:17]
	ds_read_b128 v[30:33], v0 offset:256
	ds_read_b128 v[206:209], v0 offset:16384
	ds_read_b128 v[210:213], v0 offset:16640
	s_waitcnt lgkmcnt(4)
	s_nop 0
	s_waitcnt lgkmcnt(0)
	v_mfma_f32_32x32x16_bf16 v[2:17], v[18:21], v[152:155], v[2:17]
	v_mfma_f32_32x32x16_bf16 v[2:17], v[90:93], v[184:187], v[2:17]
	v_mfma_f32_32x32x16_bf16 v[2:17], v[26:29], v[156:159], v[2:17]
	v_mfma_f32_32x32x16_bf16 v[2:17], v[30:33], v[188:191], v[2:17]
	s_setprio 0
	v_mfma_f32_32x32x16_bf16 v[18:33], v[22:25], v[128:131], 0
	s_nop 9
	v_max_f32_e32 v0, v3, v3
	ds_write_b32 v88, v1
	v_mov_b32_e32 v1, 1
	s_mov_b32 s11, 1
	s_mov_b32 s12, 0x41300000
	v_mfma_f32_32x32x16_bf16 v[18:33], v[34:37], v[160:163], v[18:33]
	v_max_f32_e32 v34, v2, v2
	v_max_f32_e32 v0, v34, v0
	v_max3_f32 v0, v0, v4, v5
	v_max3_f32 v0, v0, v6, v7
	v_max3_f32 v0, v0, v8, v9
	v_max3_f32 v0, v0, v10, v11
	v_max3_f32 v0, v0, v12, v13
	v_mfma_f32_32x32x16_bf16 v[18:33], v[38:41], v[132:135], v[18:33]
	v_max3_f32 v0, v0, v14, v15
	v_max3_f32 v0, v0, v16, v17
	v_mov_b32_e32 v34, s10
	ds_write_b32 v34, v1
	v_mfma_f32_32x32x16_bf16 v[18:33], v[42:45], v[164:167], v[18:33]
	v_mfma_f32_32x32x16_bf16 v[18:33], v[100:103], v[136:139], v[18:33]
	v_mfma_f32_32x32x16_bf16 v[18:33], v[104:107], v[168:171], v[18:33]
	v_mfma_f32_32x32x16_bf16 v[18:33], v[108:111], v[140:143], v[18:33]
	v_mfma_f32_32x32x16_bf16 v[18:33], v[112:115], v[172:175], v[18:33]
	v_mfma_f32_32x32x16_bf16 v[18:33], v[116:119], v[144:147], v[18:33]
	v_mfma_f32_32x32x16_bf16 v[18:33], v[120:123], v[176:179], v[18:33]
	v_mfma_f32_32x32x16_bf16 v[18:33], v[124:127], v[148:151], v[18:33]
	v_mfma_f32_32x32x16_bf16 v[18:33], v[194:197], v[180:183], v[18:33]
	v_mfma_f32_32x32x16_bf16 v[18:33], v[198:201], v[152:155], v[18:33]
	v_mfma_f32_32x32x16_bf16 v[18:33], v[202:205], v[184:187], v[18:33]
	v_mfma_f32_32x32x16_bf16 v[18:33], v[206:209], v[156:159], v[18:33]
	v_mfma_f32_32x32x16_bf16 v[18:33], v[210:213], v[188:191], v[18:33]
	s_nop 11
	v_max3_f32 v0, v0, v18, v19
	v_max3_f32 v0, v0, v20, v21
	v_max3_f32 v0, v0, v22, v23
	v_max3_f32 v0, v0, v24, v25
	v_max3_f32 v0, v0, v26, v27
	v_max3_f32 v0, v0, v28, v29
	v_max3_f32 v0, v0, v30, v31
	v_max3_f32 v0, v0, v32, v33
	v_mov_b32_e32 v1, v0
	s_nop 1
	v_permlane32_swap_b32_e32 v0, v1
	v_max_f32_e32 v1, v1, v1
	v_max_f32_e32 v0, v0, v0
	v_max_f32_e32 v0, v0, v1
	v_add_f32_e32 v90, 0, v0
	v_add_f32_e64 v2, -v90, v2
	v_add_f32_e64 v3, -v90, v3
	v_add_f32_e64 v4, -v90, v4
	v_add_f32_e64 v5, -v90, v5
	v_add_f32_e64 v6, -v90, v6
	v_add_f32_e64 v7, -v90, v7
	v_add_f32_e64 v8, -v90, v8
	v_add_f32_e64 v9, -v90, v9
	v_add_f32_e64 v1, -v90, v18
	v_add_f32_e64 v18, -v90, v19
	v_add_f32_e64 v19, -v90, v20
	v_add_f32_e64 v20, -v90, v21
	v_add_f32_e64 v21, -v90, v22
	v_add_f32_e64 v22, -v90, v23
	v_add_f32_e64 v23, -v90, v24
	v_add_f32_e64 v24, -v90, v25
	v_add_f32_e64 v25, -v90, v26
	v_add_f32_e64 v26, -v90, v27
	v_add_f32_e64 v27, -v90, v28
	v_add_f32_e64 v28, -v90, v29
	v_add_f32_e64 v29, -v90, v30
	v_add_f32_e64 v30, -v90, v31
	v_add_f32_e64 v31, -v90, v32
	v_add_f32_e64 v32, -v90, v33
	v_add_f32_e64 v10, -v90, v10
	v_add_f32_e64 v11, -v90, v11
	v_add_f32_e64 v12, -v90, v12
	v_add_f32_e64 v13, -v90, v13
	v_add_f32_e64 v14, -v90, v14
	v_add_f32_e64 v15, -v90, v15
	v_add_f32_e64 v16, -v90, v16
	v_add_f32_e64 v17, -v90, v17
	v_exp_f32_e32 v33, v2
	v_exp_f32_e32 v34, v3
	v_exp_f32_e32 v35, v4
	v_exp_f32_e32 v36, v5
	v_exp_f32_e32 v37, v6
	v_exp_f32_e32 v38, v7
	v_exp_f32_e32 v39, v8
	v_exp_f32_e32 v40, v9
	v_exp_f32_e32 v41, v10
	v_exp_f32_e32 v42, v11
	v_exp_f32_e32 v43, v12
	v_exp_f32_e32 v44, v13
	v_exp_f32_e32 v45, v14
	v_exp_f32_e32 v46, v15
	v_exp_f32_e32 v47, v16
	v_exp_f32_e32 v91, v17
	v_exp_f32_e32 v92, v1
	v_exp_f32_e32 v93, v18
	v_exp_f32_e32 v94, v19
	v_exp_f32_e32 v95, v20
	v_exp_f32_e32 v99, v21
	v_exp_f32_e32 v100, v22
	v_exp_f32_e32 v101, v23
	v_exp_f32_e32 v102, v24
	v_exp_f32_e32 v103, v25
	v_exp_f32_e32 v104, v26
	v_exp_f32_e32 v105, v27
	v_exp_f32_e32 v28, v28
	v_exp_f32_e32 v29, v29
	v_exp_f32_e32 v30, v30
	v_exp_f32_e32 v31, v31
	v_exp_f32_e32 v32, v32
	v_cvt_pk_bf16_f32 v12, v33, v34
	v_cvt_pk_bf16_f32 v13, v35, v36
	v_cvt_pk_bf16_f32 v14, v37, v38
	v_cvt_pk_bf16_f32 v15, v39, v40
	v_add_f32_e32 v33, 0, v33
	v_cvt_pk_bf16_f32 v16, v41, v42
	v_cvt_pk_bf16_f32 v17, v43, v44
	v_cvt_pk_bf16_f32 v18, v45, v46
	v_cvt_pk_bf16_f32 v19, v47, v91
	v_cvt_pk_bf16_f32 v20, v92, v93
	v_cvt_pk_bf16_f32 v21, v94, v95
	v_cvt_pk_bf16_f32 v22, v99, v100
	v_cvt_pk_bf16_f32 v23, v101, v102
	v_cvt_pk_bf16_f32 v24, v103, v104
	v_cvt_pk_bf16_f32 v25, v105, v28
	v_cvt_pk_bf16_f32 v26, v29, v30
	v_cvt_pk_bf16_f32 v27, v31, v32
	ds_write_b128 v89, v[12:15]
	ds_write_b128 v89, v[16:19] offset:1024
	ds_write_b128 v89, v[20:23] offset:2048
	ds_write_b128 v89, v[24:27] offset:3072
	v_add_f32_e32 v12, v33, v34
	v_add_f32_e32 v12, v12, v35
	v_add_f32_e32 v12, v12, v36
	v_add_f32_e32 v12, v12, v37
	v_add_f32_e32 v12, v12, v38
	v_add_f32_e32 v12, v12, v39
	v_add_f32_e32 v12, v12, v40
	v_add_f32_e32 v12, v12, v41
	v_add_f32_e32 v12, v12, v42
	v_add_f32_e32 v12, v12, v43
	v_add_f32_e32 v12, v12, v44
	v_add_f32_e32 v12, v12, v45
	v_add_f32_e32 v12, v12, v46
	v_add_f32_e32 v12, v12, v47
	v_add_f32_e32 v12, v12, v91
	v_add_f32_e32 v12, v12, v92
	v_add_f32_e32 v12, v12, v93
	v_add_f32_e32 v12, v12, v94
	v_add_f32_e32 v12, v12, v95
	v_add_f32_e32 v12, v12, v99
	v_add_f32_e32 v12, v12, v100
	v_add_f32_e32 v12, v12, v101
	v_add_f32_e32 v12, v12, v102
	v_add_f32_e32 v12, v12, v103
	v_add_f32_e32 v12, v12, v104
	v_add_f32_e32 v12, v12, v105
	v_add_f32_e32 v12, v12, v28
	v_add_f32_e32 v12, v12, v29
	v_add_f32_e32 v12, v12, v30
	s_waitcnt lgkmcnt(0)
	s_barrier
	v_add_f32_e32 v12, v12, v31
	v_xor_b32_e32 v0, 0x80000000, v90
	v_add_f32_e32 v12, v12, v32
	v_mov_b32_e32 v1, v0
	v_mov_b32_e32 v2, v0
	v_mov_b32_e32 v3, v0
	v_mov_b32_e32 v4, v0
	v_mov_b32_e32 v5, v0
	v_mov_b32_e32 v6, v0
	v_mov_b32_e32 v7, v0
	v_mov_b32_e32 v8, v0
	v_mov_b32_e32 v9, v0
	v_mov_b32_e32 v10, v0
	v_mov_b32_e32 v11, v0
	v_add_f32_e32 v99, 0, v12
	v_mov_b32_e32 v12, v0
	v_mov_b32_e32 v13, v0
	v_mov_b32_e32 v14, v0
	v_mov_b32_e32 v15, v0
	s_branch .LBB1_21
